# stack: v26 + out-proj first-trip peel + K-loop header tests before the closing barrier + trimmed fp8 hazard padding
# baseline (speedup 1.0000x reference)
; #define PG8_STAGE(bufoff, gbase, voff) do { _Pragma("unroll") for (int _i = 0; _i < 2; ++_i) \
;         __builtin_amdgcn_global_load_lds((const unsigned*)((const char*)(gbase) + (voff)[_i]), (PG8_LAS unsigned*)(lds + (bufoff) + ldsw + _i * 8192), 16, 0, 0); } while (0)
; #define PG8_STAGE_A(bufoff, kbase, h, gv) do { if constexpr (GATHER) { PG8_STAGE(bufoff, kbase, (gv)[h]); } else { PG8_STAGE(bufoff, (kbase) + (h) * hstep, voffA); } } while (0)
; #define PG8_WAIT_V(n) asm volatile("s_waitcnt vmcnt(" #n ")" ::: "memory")
; #define PG8_WAIT_L(n) asm volatile("s_waitcnt lgkmcnt(" #n ")" ::: "memory")
; #define PG8_BAR __builtin_amdgcn_s_barrier()
; #define PG8_SCHED __builtin_amdgcn_sched_barrier(0)
; template <class Epi, class Sched, bool ALIGN_EPI = false, bool SP2 = false, bool FP8 = false, bool GATHER = false>
; __device__ __forceinline__ void gemm_phase(PG8_LAS unsigned char* lds, const Gemm g, const Sched& S, const Epi& E) {
;     ...
;             PG8_LDB(B0, 0, 0); PG8_LDB(B1, 0, 1); PG8_SCHED; PG8_LDA(At, 0, 0); PG8_STAGE_A(PG8_SA(1, 1), a1, 1, gcur);
;             PG8_WAIT_V(8); PG8_WAIT_L(0); PG8_BAR; PG8_MMA(0, 0, At, B0); PG8_MMA(0, 1, At, B1); PG8_BAR; PG8_SCHED;
;             PG8_LDA(At, 0, 1); PG8_STAGE(PG8_SB(0, 0), b2, voffB); PG8_STAGE(PG8_SB(0, 1), b2 + hstep, voffB); PG8_STAGE_A(PG8_SA(0, 0), a2, 0, gsel);
;             PG8_WAIT_V(8); PG8_WAIT_L(0); PG8_BAR; PG8_MMA(1, 0, At, B0); PG8_MMA(1, 1, At, B1); PG8_BAR; PG8_SCHED;
.Lpeel592_body:
	v_add_u32_e32 v136, s82, v169
	ds_read_b128 v[124:127], v136
	ds_read_b128 v[128:131], v136 offset:1024
	ds_read_b128 v[132:135], v136 offset:2048
	ds_read_b128 v[164:167], v136 offset:3072
	v_add_u32_e32 v136, s83, v169
	ds_read_b128 v[172:175], v136
	ds_read_b128 v[176:179], v136 offset:1024
	ds_read_b128 v[180:183], v136 offset:2048
	ds_read_b128 v[184:187], v136 offset:3072
	s_add_u32 s60, s56, 0xfffc0080
	s_addc_u32 s61, s57, -1
	s_and_b64 s[58:59], s[58:59], exec
	s_cselect_b32 s61, s61, s47
	s_cselect_b32 s60, s60, s85
	s_cselect_b32 s59, s88, s86
	s_cselect_b32 s58, s55, s87
	v_lshl_add_u64 v[136:137], s[56:57], 0, v[154:155]
	s_add_i32 m0, s53, 0xc000
	ds_read_b128 v[188:191], v170
	ds_read_b128 v[192:195], v170 offset:1024
	ds_read_b128 v[196:199], v170 offset:2048
	ds_read_b128 v[200:203], v170 offset:3072
	ds_read_b128 v[204:207], v170 offset:4096
	ds_read_b128 v[208:211], v170 offset:5120
	ds_read_b128 v[212:215], v170 offset:6144
	ds_read_b128 v[216:219], v170 offset:7168
	global_load_lds_dwordx4 v[136:137], off
	v_lshl_add_u64 v[136:137], s[56:57], 0, v[156:157]
	s_add_i32 m0, s53, 0xe000
	s_nop 0
	global_load_lds_dwordx4 v[136:137], off
	s_waitcnt vmcnt(8)
	s_waitcnt lgkmcnt(0)
	s_barrier
	s_setprio 1
	s_waitcnt lgkmcnt(0)
	v_mfma_f32_16x16x32_bf16 v[142:145], v[124:127], v[188:191], 0
	v_mfma_f32_16x16x32_bf16 v[136:139], v[132:135], v[188:191], 0
	v_mfma_f32_16x16x32_bf16 v[118:121], v[124:127], v[196:199], 0
	v_mfma_f32_16x16x32_bf16 v[106:109], v[132:135], v[196:199], 0
	v_mfma_f32_16x16x32_bf16 v[102:105], v[124:127], v[204:207], 0
	v_mfma_f32_16x16x32_bf16 v[90:93], v[132:135], v[204:207], 0
	v_mfma_f32_16x16x32_bf16 v[86:89], v[124:127], v[212:215], 0
	v_mfma_f32_16x16x32_bf16 v[74:77], v[132:135], v[212:215], 0
	v_mfma_f32_16x16x32_bf16 v[142:145], v[128:131], v[192:195], v[142:145]
	v_mfma_f32_16x16x32_bf16 v[136:139], v[164:167], v[192:195], v[136:139]
	v_mfma_f32_16x16x32_bf16 v[118:121], v[128:131], v[200:203], v[118:121]
	v_mfma_f32_16x16x32_bf16 v[106:109], v[164:167], v[200:203], v[106:109]
	v_mfma_f32_16x16x32_bf16 v[102:105], v[128:131], v[208:211], v[102:105]
	v_mfma_f32_16x16x32_bf16 v[90:93], v[164:167], v[208:211], v[90:93]
	v_mfma_f32_16x16x32_bf16 v[86:89], v[128:131], v[216:219], v[86:89]
	v_mfma_f32_16x16x32_bf16 v[74:77], v[164:167], v[216:219], v[74:77]
	s_setprio 0
	s_setprio 1
	v_mfma_f32_16x16x32_bf16 v[114:117], v[172:175], v[188:191], 0
	v_mfma_f32_16x16x32_bf16 v[110:113], v[180:183], v[188:191], 0
	v_mfma_f32_16x16x32_bf16 v[98:101], v[172:175], v[196:199], 0
	v_mfma_f32_16x16x32_bf16 v[94:97], v[180:183], v[196:199], 0
	v_mfma_f32_16x16x32_bf16 v[82:85], v[172:175], v[204:207], 0
	v_mfma_f32_16x16x32_bf16 v[78:81], v[180:183], v[204:207], 0
	v_mfma_f32_16x16x32_bf16 v[70:73], v[172:175], v[212:215], 0
	v_mfma_f32_16x16x32_bf16 v[66:69], v[180:183], v[212:215], 0
	v_mfma_f32_16x16x32_bf16 v[114:117], v[176:179], v[192:195], v[114:117]
	v_mfma_f32_16x16x32_bf16 v[110:113], v[184:187], v[192:195], v[110:113]
	v_mfma_f32_16x16x32_bf16 v[98:101], v[176:179], v[200:203], v[98:101]
	v_mfma_f32_16x16x32_bf16 v[94:97], v[184:187], v[200:203], v[94:97]
	v_mfma_f32_16x16x32_bf16 v[82:85], v[176:179], v[208:211], v[82:85]
	v_mfma_f32_16x16x32_bf16 v[78:81], v[184:187], v[208:211], v[78:81]
	v_mfma_f32_16x16x32_bf16 v[70:73], v[176:179], v[216:219], v[70:73]
	v_mfma_f32_16x16x32_bf16 v[66:69], v[184:187], v[216:219], v[66:69]
	s_setprio 0
	s_barrier
	s_add_i32 s90, s82, s67
	v_lshl_add_u64 v[220:221], s[58:59], 0, v[150:151]
	s_mov_b32 m0, s90
	ds_read_b128 v[188:191], v170 offset:16384
	ds_read_b128 v[192:195], v170 offset:17408
	ds_read_b128 v[196:199], v170 offset:18432
	ds_read_b128 v[200:203], v170 offset:19456
	ds_read_b128 v[204:207], v170 offset:20480
	ds_read_b128 v[208:211], v170 offset:21504
	ds_read_b128 v[212:215], v170 offset:22528
	ds_read_b128 v[216:219], v170 offset:23552
	global_load_lds_dwordx4 v[220:221], off
	s_add_i32 m0, s90, 0x2000
	s_add_u32 s90, s58, 0x40000
	v_lshl_add_u64 v[222:223], s[58:59], 0, v[146:147]
	s_addc_u32 s91, s59, 0
	s_add_i32 s92, s83, s67
	global_load_lds_dwordx4 v[222:223], off
	v_lshl_add_u64 v[140:141], s[90:91], 0, v[150:151]
	s_mov_b32 m0, s92
	v_lshl_add_u64 v[224:225], s[60:61], 0, v[152:153]
	global_load_lds_dwordx4 v[140:141], off
	v_lshl_add_u64 v[140:141], s[90:91], 0, v[146:147]
	s_add_i32 m0, s92, 0x2000
	v_lshl_add_u64 v[226:227], s[60:61], 0, v[148:149]
	global_load_lds_dwordx4 v[140:141], off
	s_mov_b32 m0, s53
	s_nop 0
	global_load_lds_dwordx4 v[224:225], off
	s_mov_b32 m0, s70
	s_nop 0
	global_load_lds_dwordx4 v[226:227], off
	s_waitcnt vmcnt(8)
	s_waitcnt lgkmcnt(0)
	s_barrier
; #define PG8_STAGE(bufoff, gbase, voff) do { _Pragma("unroll") for (int _i = 0; _i < 2; ++_i) \
;         __builtin_amdgcn_global_load_lds((const unsigned*)((const char*)(gbase) + (voff)[_i]), (PG8_LAS unsigned*)(lds + (bufoff) + ldsw + _i * 8192), 16, 0, 0); } while (0)
; #define PG8_STAGE_A(bufoff, kbase, h, gv) do { if constexpr (GATHER) { PG8_STAGE(bufoff, kbase, (gv)[h]); } else { PG8_STAGE(bufoff, (kbase) + (h) * hstep, voffA); } } while (0)
; #define PG8_WAIT_V(n) asm volatile("s_waitcnt vmcnt(" #n ")" ::: "memory")
; #define PG8_WAIT_L(n) asm volatile("s_waitcnt lgkmcnt(" #n ")" ::: "memory")
; #define PG8_BAR __builtin_amdgcn_s_barrier()
; #define PG8_SCHED __builtin_amdgcn_sched_barrier(0)
; template <class Epi, class Sched, bool ALIGN_EPI = false, bool SP2 = false, bool FP8 = false, bool GATHER = false>
; __device__ __forceinline__ void gemm_phase(PG8_LAS unsigned char* lds, const Gemm g, const Sched& S, const Epi& E) {
;     ...
;             PG8_WAIT_V(8); PG8_WAIT_L(0); PG8_BAR; PG8_MMA(1, 0, At, B0); PG8_MMA(1, 1, At, B1); PG8_BAR; PG8_SCHED;
;             PG8_LDB(B0, 1, 0); PG8_LDB(B1, 1, 1); PG8_SCHED; PG8_LDA(At, 1, 0); PG8_STAGE_A(PG8_SA(0, 1), a2, 1, gsel);
;             PG8_WAIT_V(8); PG8_WAIT_L(0); PG8_BAR; PG8_MMA(0, 0, At, B0); PG8_MMA(0, 1, At, B1); PG8_BAR; PG8_SCHED;
;             PG8_LDA(At, 1, 1); PG8_STAGE(PG8_SB(1, 0), b3, voffB); PG8_STAGE(PG8_SB(1, 1), b3 + hstep, voffB); PG8_STAGE_A(PG8_SA(1, 0), a3, 0, gsel);
	s_setprio 1
	s_waitcnt lgkmcnt(0)
	v_mfma_f32_16x16x32_bf16 v[62:65], v[124:127], v[188:191], 0
	v_mfma_f32_16x16x32_bf16 v[58:61], v[132:135], v[188:191], 0
	v_mfma_f32_16x16x32_bf16 v[54:57], v[124:127], v[196:199], 0
	v_mfma_f32_16x16x32_bf16 v[42:45], v[132:135], v[196:199], 0
	v_mfma_f32_16x16x32_bf16 v[38:41], v[124:127], v[204:207], 0
	v_mfma_f32_16x16x32_bf16 v[26:29], v[132:135], v[204:207], 0
	v_mfma_f32_16x16x32_bf16 v[22:25], v[124:127], v[212:215], 0
	v_mfma_f32_16x16x32_bf16 v[10:13], v[132:135], v[212:215], 0
	v_mfma_f32_16x16x32_bf16 v[62:65], v[128:131], v[192:195], v[62:65]
	v_mfma_f32_16x16x32_bf16 v[58:61], v[164:167], v[192:195], v[58:61]
	v_mfma_f32_16x16x32_bf16 v[54:57], v[128:131], v[200:203], v[54:57]
	v_mfma_f32_16x16x32_bf16 v[42:45], v[164:167], v[200:203], v[42:45]
	v_mfma_f32_16x16x32_bf16 v[38:41], v[128:131], v[208:211], v[38:41]
	v_mfma_f32_16x16x32_bf16 v[26:29], v[164:167], v[208:211], v[26:29]
	v_mfma_f32_16x16x32_bf16 v[22:25], v[128:131], v[216:219], v[22:25]
	v_mfma_f32_16x16x32_bf16 v[10:13], v[164:167], v[216:219], v[10:13]
	s_setprio 0
	s_setprio 1
	v_mfma_f32_16x16x32_bf16 v[50:53], v[172:175], v[188:191], 0
	v_mfma_f32_16x16x32_bf16 v[46:49], v[180:183], v[188:191], 0
	v_mfma_f32_16x16x32_bf16 v[34:37], v[172:175], v[196:199], 0
	v_mfma_f32_16x16x32_bf16 v[30:33], v[180:183], v[196:199], 0
	v_mfma_f32_16x16x32_bf16 v[18:21], v[172:175], v[204:207], 0
	v_mfma_f32_16x16x32_bf16 v[14:17], v[180:183], v[204:207], 0
	v_mfma_f32_16x16x32_bf16 v[6:9], v[172:175], v[212:215], 0
	v_mfma_f32_16x16x32_bf16 v[2:5], v[180:183], v[212:215], 0
	v_mfma_f32_16x16x32_bf16 v[50:53], v[176:179], v[192:195], v[50:53]
	v_mfma_f32_16x16x32_bf16 v[46:49], v[184:187], v[192:195], v[46:49]
	v_mfma_f32_16x16x32_bf16 v[34:37], v[176:179], v[200:203], v[34:37]
	v_mfma_f32_16x16x32_bf16 v[30:33], v[184:187], v[200:203], v[30:33]
	v_mfma_f32_16x16x32_bf16 v[18:21], v[176:179], v[208:211], v[18:21]
	v_mfma_f32_16x16x32_bf16 v[14:17], v[184:187], v[208:211], v[14:17]
	v_mfma_f32_16x16x32_bf16 v[6:9], v[176:179], v[216:219], v[6:9]
	v_mfma_f32_16x16x32_bf16 v[2:5], v[184:187], v[216:219], v[2:5]
	s_setprio 0
	s_barrier
	s_add_i32 s90, 0, 0x18000
	v_add_u32_e32 v140, s90, v169
	s_add_i32 s91, 0, 0x1c000
	ds_read_b128 v[124:127], v140
	ds_read_b128 v[128:131], v140 offset:1024
	ds_read_b128 v[132:135], v140 offset:2048
	ds_read_b128 v[164:167], v140 offset:3072
	v_add_u32_e32 v140, s91, v169
	ds_read_b128 v[172:175], v140
	ds_read_b128 v[176:179], v140 offset:1024
	ds_read_b128 v[180:183], v140 offset:2048
	ds_read_b128 v[184:187], v140 offset:3072
	s_add_u32 s60, s60, 0x40000
	s_addc_u32 s61, s61, 0
	s_mov_b32 m0, s71
	v_lshl_add_u64 v[140:141], s[60:61], 0, v[152:153]
	ds_read_b128 v[188:191], v170 offset:32768
	ds_read_b128 v[192:195], v170 offset:33792
	ds_read_b128 v[196:199], v170 offset:34816
	ds_read_b128 v[200:203], v170 offset:35840
	ds_read_b128 v[204:207], v170 offset:36864
	ds_read_b128 v[208:211], v170 offset:37888
	ds_read_b128 v[212:215], v170 offset:38912
	ds_read_b128 v[216:219], v170 offset:39936
	global_load_lds_dwordx4 v[140:141], off
	v_lshl_add_u64 v[140:141], s[60:61], 0, v[148:149]
	s_mov_b32 m0, s72
	s_nop 0
	global_load_lds_dwordx4 v[140:141], off
	s_waitcnt vmcnt(8)
	s_waitcnt lgkmcnt(0)
	s_barrier
	s_setprio 1
	s_waitcnt lgkmcnt(0)
	v_mfma_f32_16x16x32_bf16 v[140:143], v[124:127], v[188:191], v[142:145]
	v_mfma_f32_16x16x32_bf16 v[136:139], v[132:135], v[188:191], v[136:139]
	v_mfma_f32_16x16x32_bf16 v[118:121], v[124:127], v[196:199], v[118:121]
	v_mfma_f32_16x16x32_bf16 v[106:109], v[132:135], v[196:199], v[106:109]
	v_mfma_f32_16x16x32_bf16 v[102:105], v[124:127], v[204:207], v[102:105]
	v_mfma_f32_16x16x32_bf16 v[90:93], v[132:135], v[204:207], v[90:93]
	v_mfma_f32_16x16x32_bf16 v[86:89], v[124:127], v[212:215], v[86:89]
	v_mfma_f32_16x16x32_bf16 v[74:77], v[132:135], v[212:215], v[74:77]
	v_mfma_f32_16x16x32_bf16 v[142:145], v[128:131], v[192:195], v[140:143]
	v_mfma_f32_16x16x32_bf16 v[138:141], v[164:167], v[192:195], v[136:139]
	v_mfma_f32_16x16x32_bf16 v[118:121], v[128:131], v[200:203], v[118:121]
	v_mfma_f32_16x16x32_bf16 v[106:109], v[164:167], v[200:203], v[106:109]
	v_mfma_f32_16x16x32_bf16 v[102:105], v[128:131], v[208:211], v[102:105]
	v_mfma_f32_16x16x32_bf16 v[90:93], v[164:167], v[208:211], v[90:93]
	v_mfma_f32_16x16x32_bf16 v[86:89], v[128:131], v[216:219], v[86:89]
	v_mfma_f32_16x16x32_bf16 v[74:77], v[164:167], v[216:219], v[74:77]
	s_setprio 0
	s_setprio 1
	v_mfma_f32_16x16x32_bf16 v[114:117], v[172:175], v[188:191], v[114:117]
	v_mfma_f32_16x16x32_bf16 v[110:113], v[180:183], v[188:191], v[110:113]
	v_mfma_f32_16x16x32_bf16 v[98:101], v[172:175], v[196:199], v[98:101]
	v_mfma_f32_16x16x32_bf16 v[94:97], v[180:183], v[196:199], v[94:97]
	v_mfma_f32_16x16x32_bf16 v[82:85], v[172:175], v[204:207], v[82:85]
	v_mfma_f32_16x16x32_bf16 v[78:81], v[180:183], v[204:207], v[78:81]
	v_mfma_f32_16x16x32_bf16 v[70:73], v[172:175], v[212:215], v[70:73]
	v_mfma_f32_16x16x32_bf16 v[66:69], v[180:183], v[212:215], v[66:69]
	v_mfma_f32_16x16x32_bf16 v[114:117], v[176:179], v[192:195], v[114:117]
	v_mfma_f32_16x16x32_bf16 v[110:113], v[184:187], v[192:195], v[110:113]
	v_mfma_f32_16x16x32_bf16 v[98:101], v[176:179], v[200:203], v[98:101]
	v_mfma_f32_16x16x32_bf16 v[94:97], v[184:187], v[200:203], v[94:97]
	v_mfma_f32_16x16x32_bf16 v[82:85], v[176:179], v[208:211], v[82:85]
	v_mfma_f32_16x16x32_bf16 v[78:81], v[184:187], v[208:211], v[78:81]
	v_mfma_f32_16x16x32_bf16 v[70:73], v[176:179], v[216:219], v[70:73]
	v_mfma_f32_16x16x32_bf16 v[66:69], v[184:187], v[216:219], v[66:69]
	s_setprio 0
	s_barrier
; #define PG8_STAGE(bufoff, gbase, voff) do { _Pragma("unroll") for (int _i = 0; _i < 2; ++_i) \
;         __builtin_amdgcn_global_load_lds((const unsigned*)((const char*)(gbase) + (voff)[_i]), (PG8_LAS unsigned*)(lds + (bufoff) + ldsw + _i * 8192), 16, 0, 0); } while (0)
; #define PG8_STAGE_A(bufoff, kbase, h, gv) do { if constexpr (GATHER) { PG8_STAGE(bufoff, kbase, (gv)[h]); } else { PG8_STAGE(bufoff, (kbase) + (h) * hstep, voffA); } } while (0)
; #define PG8_WAIT_V(n) asm volatile("s_waitcnt vmcnt(" #n ")" ::: "memory")
; #define PG8_WAIT_L(n) asm volatile("s_waitcnt lgkmcnt(" #n ")" ::: "memory")
; #define PG8_BAR __builtin_amdgcn_s_barrier()
; #define PG8_SCHED __builtin_amdgcn_sched_barrier(0)
; template <class Epi, class Sched, bool ALIGN_EPI = false, bool SP2 = false, bool FP8 = false, bool GATHER = false>
; __device__ __forceinline__ void gemm_phase(PG8_LAS unsigned char* lds, const Gemm g, const Sched& S, const Epi& E) {
;     ...
;         for (int t = 0; t < nt; t += 2) {
;             const bool last = (t == nt - 2);
;             const char* a1 = cA + (size_t)(t + 1) * kstep;
;             const char* a2 = last ? nA : cA + (size_t)(t + 2) * kstep; const char* b2 = last ? nB : cB + (size_t)(t + 2) * kstep;
;             const char* a3 = a2 + kstep; const char* b3 = b2 + kstep;
;             if (last && has_next) S.a_ready(nxt);
;             if (last) E.pre(cur, wid, lane);
;     ...
;             PG8_LDA(At, 1, 1); PG8_STAGE(PG8_SB(1, 0), b3, voffB); PG8_STAGE(PG8_SB(1, 1), b3 + hstep, voffB); PG8_STAGE_A(PG8_SA(1, 0), a3, 0, gsel);
;             PG8_WAIT_V(8); PG8_WAIT_L(0); PG8_BAR; PG8_MMA(1, 0, At, B0); PG8_MMA(1, 1, At, B1); PG8_BAR; PG8_SCHED;
	s_add_i32 s60, s90, s67
	v_lshl_add_u64 v[136:137], v[220:221], 0, s[18:19]
	s_mov_b32 m0, s60
	ds_read_b128 v[188:191], v170 offset:49152
	ds_read_b128 v[192:195], v170 offset:50176
	ds_read_b128 v[196:199], v170 offset:51200
	ds_read_b128 v[200:203], v170 offset:52224
	ds_read_b128 v[204:207], v170 offset:53248
	ds_read_b128 v[208:211], v170 offset:54272
	ds_read_b128 v[212:215], v170 offset:55296
	ds_read_b128 v[216:219], v170 offset:56320
	global_load_lds_dwordx4 v[136:137], off
	s_add_i32 m0, s60, 0x2000
	s_add_u32 s58, s58, 0x40080
	v_lshl_add_u64 v[136:137], v[222:223], 0, s[18:19]
	s_addc_u32 s59, s59, 0
	s_add_i32 s60, s91, s67
	global_load_lds_dwordx4 v[136:137], off
	v_lshl_add_u64 v[136:137], s[58:59], 0, v[150:151]
	s_mov_b32 m0, s60
	s_nop 0
	global_load_lds_dwordx4 v[136:137], off
	v_lshl_add_u64 v[136:137], s[58:59], 0, v[146:147]
	s_add_i32 m0, s60, 0x2000
	s_nop 0
	global_load_lds_dwordx4 v[136:137], off
	v_lshl_add_u64 v[136:137], v[224:225], 0, s[18:19]
	s_mov_b32 m0, s78
	s_nop 0
	global_load_lds_dwordx4 v[136:137], off
	v_lshl_add_u64 v[136:137], v[226:227], 0, s[18:19]
	s_mov_b32 m0, s79
	s_nop 0
	global_load_lds_dwordx4 v[136:137], off
	s_waitcnt vmcnt(8)
	s_waitcnt lgkmcnt(0)
	s_barrier
	s_setprio 1
	s_waitcnt lgkmcnt(0)
	v_mfma_f32_16x16x32_bf16 v[62:65], v[124:127], v[188:191], v[62:65]
	v_mfma_f32_16x16x32_bf16 v[58:61], v[132:135], v[188:191], v[58:61]
	v_mfma_f32_16x16x32_bf16 v[54:57], v[124:127], v[196:199], v[54:57]
	v_mfma_f32_16x16x32_bf16 v[42:45], v[132:135], v[196:199], v[42:45]
	v_mfma_f32_16x16x32_bf16 v[38:41], v[124:127], v[204:207], v[38:41]
	v_mfma_f32_16x16x32_bf16 v[26:29], v[132:135], v[204:207], v[26:29]
	v_mfma_f32_16x16x32_bf16 v[22:25], v[124:127], v[212:215], v[22:25]
	v_mfma_f32_16x16x32_bf16 v[10:13], v[132:135], v[212:215], v[10:13]
	v_mfma_f32_16x16x32_bf16 v[62:65], v[128:131], v[192:195], v[62:65]
	v_mfma_f32_16x16x32_bf16 v[58:61], v[164:167], v[192:195], v[58:61]
	v_mfma_f32_16x16x32_bf16 v[54:57], v[128:131], v[200:203], v[54:57]
	v_mfma_f32_16x16x32_bf16 v[42:45], v[164:167], v[200:203], v[42:45]
	v_mfma_f32_16x16x32_bf16 v[38:41], v[128:131], v[208:211], v[38:41]
	v_mfma_f32_16x16x32_bf16 v[26:29], v[164:167], v[208:211], v[26:29]
	v_mfma_f32_16x16x32_bf16 v[22:25], v[128:131], v[216:219], v[22:25]
	v_mfma_f32_16x16x32_bf16 v[10:13], v[164:167], v[216:219], v[10:13]
	s_setprio 0
	s_setprio 1
	v_mfma_f32_16x16x32_bf16 v[50:53], v[172:175], v[188:191], v[50:53]
	v_mfma_f32_16x16x32_bf16 v[46:49], v[180:183], v[188:191], v[46:49]
	v_mfma_f32_16x16x32_bf16 v[34:37], v[172:175], v[196:199], v[34:37]
	v_mfma_f32_16x16x32_bf16 v[30:33], v[180:183], v[196:199], v[30:33]
	v_mfma_f32_16x16x32_bf16 v[18:21], v[172:175], v[204:207], v[18:21]
	v_mfma_f32_16x16x32_bf16 v[14:17], v[180:183], v[204:207], v[14:17]
	v_mfma_f32_16x16x32_bf16 v[6:9], v[172:175], v[212:215], v[6:9]
	v_mfma_f32_16x16x32_bf16 v[2:5], v[180:183], v[212:215], v[2:5]
	v_mfma_f32_16x16x32_bf16 v[50:53], v[176:179], v[192:195], v[50:53]
	v_mfma_f32_16x16x32_bf16 v[46:49], v[184:187], v[192:195], v[46:49]
	v_mfma_f32_16x16x32_bf16 v[34:37], v[176:179], v[200:203], v[34:37]
	v_mfma_f32_16x16x32_bf16 v[30:33], v[184:187], v[200:203], v[30:33]
	v_mfma_f32_16x16x32_bf16 v[18:21], v[176:179], v[208:211], v[18:21]
	v_mfma_f32_16x16x32_bf16 v[14:17], v[184:187], v[208:211], v[14:17]
	v_mfma_f32_16x16x32_bf16 v[6:9], v[176:179], v[216:219], v[6:9]
	v_mfma_f32_16x16x32_bf16 v[2:5], v[184:187], v[216:219], v[2:5]
	s_setprio 0
	s_add_i32 s89, s89, 2
	s_add_u32 s56, s56, 0x100
	s_addc_u32 s57, s57, 0
	s_add_u32 s55, s55, 0x100
	s_addc_u32 s88, s88, 0
	s_cmp_gt_u32 s89, 13
	s_cbranch_scc1 .Lrot592_exit
	s_cmp_lg_u32 s89, 12
	s_cselect_b64 s[58:59], -1, 0
	s_or_b64 s[60:61], s[58:59], s[20:21]
	s_and_b64 vcc, exec, s[60:61]
	s_cbranch_vccnz .Lrot592_head
	s_barrier
	s_branch .LBB0_593

; #define PG8_STAGE(bufoff, gbase, voff) do { _Pragma("unroll") for (int _i = 0; _i < 2; ++_i) \
;         __builtin_amdgcn_global_load_lds((const unsigned*)((const char*)(gbase) + (voff)[_i]), (PG8_LAS unsigned*)(lds + (bufoff) + ldsw + _i * 8192), 16, 0, 0); } while (0)
; #define PG8_STAGE_A(bufoff, kbase, h, gv) do { if constexpr (GATHER) { PG8_STAGE(bufoff, kbase, (gv)[h]); } else { PG8_STAGE(bufoff, (kbase) + (h) * hstep, voffA); } } while (0)
; #define PG8_WAIT_V(n) asm volatile("s_waitcnt vmcnt(" #n ")" ::: "memory")
; #define PG8_WAIT_L(n) asm volatile("s_waitcnt lgkmcnt(" #n ")" ::: "memory")
; #define PG8_BAR __builtin_amdgcn_s_barrier()
; #define PG8_SCHED __builtin_amdgcn_sched_barrier(0)
; template <class Epi, class Sched, bool ALIGN_EPI = false, bool SP2 = false, bool FP8 = false, bool GATHER = false>
; __device__ __forceinline__ void gemm_phase(PG8_LAS unsigned char* lds, const Gemm g, const Sched& S, const Epi& E) {
;     ...
;             PG8_LDB(B0, 0, 0); PG8_LDB(B1, 0, 1); PG8_SCHED; PG8_LDA(At, 0, 0); PG8_STAGE_A(PG8_SA(1, 1), a1, 1, gcur);
;             PG8_WAIT_V(8); PG8_WAIT_L(0); PG8_BAR; PG8_MMA(0, 0, At, B0); PG8_MMA(0, 1, At, B1); PG8_BAR; PG8_SCHED;
;             PG8_LDA(At, 0, 1); PG8_STAGE(PG8_SB(0, 0), b2, voffB); PG8_STAGE(PG8_SB(0, 1), b2 + hstep, voffB); PG8_STAGE_A(PG8_SA(0, 0), a2, 0, gsel);
;             PG8_WAIT_V(8); PG8_WAIT_L(0); PG8_BAR; PG8_MMA(1, 0, At, B0); PG8_MMA(1, 1, At, B1); PG8_BAR; PG8_SCHED;
.Lpeel1497_body:
	v_add_u32_e32 v136, s79, v169
	ds_read_b128 v[124:127], v136
	ds_read_b128 v[128:131], v136 offset:1024
	ds_read_b128 v[132:135], v136 offset:2048
	ds_read_b128 v[164:167], v136 offset:3072
	v_add_u32_e32 v136, s80, v169
	ds_read_b128 v[172:175], v136
	ds_read_b128 v[176:179], v136 offset:1024
	ds_read_b128 v[180:183], v136 offset:2048
	ds_read_b128 v[184:187], v136 offset:3072
	s_add_u32 s58, s54, 0xfffc0080
	s_addc_u32 s59, s55, -1
	s_and_b64 s[56:57], s[56:57], exec
	s_cselect_b32 s59, s59, s45
	s_cselect_b32 s58, s58, s82
	s_cselect_b32 s57, s85, s83
	s_cselect_b32 s56, s53, s84
	v_lshl_add_u64 v[136:137], s[54:55], 0, v[154:155]
	s_add_i32 m0, s51, 0xc000
	ds_read_b128 v[188:191], v170
	ds_read_b128 v[192:195], v170 offset:1024
	ds_read_b128 v[196:199], v170 offset:2048
	ds_read_b128 v[200:203], v170 offset:3072
	ds_read_b128 v[204:207], v170 offset:4096
	ds_read_b128 v[208:211], v170 offset:5120
	ds_read_b128 v[212:215], v170 offset:6144
	ds_read_b128 v[216:219], v170 offset:7168
	global_load_lds_dwordx4 v[136:137], off
	v_lshl_add_u64 v[136:137], s[54:55], 0, v[156:157]
	s_add_i32 m0, s51, 0xe000
	s_nop 0
	global_load_lds_dwordx4 v[136:137], off
	s_waitcnt vmcnt(8)
	s_waitcnt lgkmcnt(0)
	s_barrier
	s_setprio 1
	s_waitcnt lgkmcnt(0)
	v_mfma_f32_16x16x32_bf16 v[142:145], v[124:127], v[188:191], 0
	v_mfma_f32_16x16x32_bf16 v[136:139], v[132:135], v[188:191], 0
	v_mfma_f32_16x16x32_bf16 v[118:121], v[124:127], v[196:199], 0
	v_mfma_f32_16x16x32_bf16 v[106:109], v[132:135], v[196:199], 0
	v_mfma_f32_16x16x32_bf16 v[102:105], v[124:127], v[204:207], 0
	v_mfma_f32_16x16x32_bf16 v[90:93], v[132:135], v[204:207], 0
	v_mfma_f32_16x16x32_bf16 v[86:89], v[124:127], v[212:215], 0
	v_mfma_f32_16x16x32_bf16 v[74:77], v[132:135], v[212:215], 0
	v_mfma_f32_16x16x32_bf16 v[142:145], v[128:131], v[192:195], v[142:145]
	v_mfma_f32_16x16x32_bf16 v[136:139], v[164:167], v[192:195], v[136:139]
	v_mfma_f32_16x16x32_bf16 v[118:121], v[128:131], v[200:203], v[118:121]
	v_mfma_f32_16x16x32_bf16 v[106:109], v[164:167], v[200:203], v[106:109]
	v_mfma_f32_16x16x32_bf16 v[102:105], v[128:131], v[208:211], v[102:105]
	v_mfma_f32_16x16x32_bf16 v[90:93], v[164:167], v[208:211], v[90:93]
	v_mfma_f32_16x16x32_bf16 v[86:89], v[128:131], v[216:219], v[86:89]
	v_mfma_f32_16x16x32_bf16 v[74:77], v[164:167], v[216:219], v[74:77]
	s_setprio 0
	s_setprio 1
	v_mfma_f32_16x16x32_bf16 v[114:117], v[172:175], v[188:191], 0
	v_mfma_f32_16x16x32_bf16 v[110:113], v[180:183], v[188:191], 0
	v_mfma_f32_16x16x32_bf16 v[98:101], v[172:175], v[196:199], 0
	v_mfma_f32_16x16x32_bf16 v[94:97], v[180:183], v[196:199], 0
	v_mfma_f32_16x16x32_bf16 v[82:85], v[172:175], v[204:207], 0
	v_mfma_f32_16x16x32_bf16 v[78:81], v[180:183], v[204:207], 0
	v_mfma_f32_16x16x32_bf16 v[70:73], v[172:175], v[212:215], 0
	v_mfma_f32_16x16x32_bf16 v[66:69], v[180:183], v[212:215], 0
	v_mfma_f32_16x16x32_bf16 v[114:117], v[176:179], v[192:195], v[114:117]
	v_mfma_f32_16x16x32_bf16 v[110:113], v[184:187], v[192:195], v[110:113]
	v_mfma_f32_16x16x32_bf16 v[98:101], v[176:179], v[200:203], v[98:101]
	v_mfma_f32_16x16x32_bf16 v[94:97], v[184:187], v[200:203], v[94:97]
	v_mfma_f32_16x16x32_bf16 v[82:85], v[176:179], v[208:211], v[82:85]
	v_mfma_f32_16x16x32_bf16 v[78:81], v[184:187], v[208:211], v[78:81]
	v_mfma_f32_16x16x32_bf16 v[70:73], v[176:179], v[216:219], v[70:73]
	v_mfma_f32_16x16x32_bf16 v[66:69], v[184:187], v[216:219], v[66:69]
	s_setprio 0
	s_barrier
	s_add_i32 s87, s79, s66
	v_lshl_add_u64 v[220:221], s[56:57], 0, v[148:149]
	s_mov_b32 m0, s87
	ds_read_b128 v[188:191], v170 offset:16384
	ds_read_b128 v[192:195], v170 offset:17408
	ds_read_b128 v[196:199], v170 offset:18432
	ds_read_b128 v[200:203], v170 offset:19456
	ds_read_b128 v[204:207], v170 offset:20480
	ds_read_b128 v[208:211], v170 offset:21504
	ds_read_b128 v[212:215], v170 offset:22528
	ds_read_b128 v[216:219], v170 offset:23552
	global_load_lds_dwordx4 v[220:221], off
	s_add_i32 m0, s87, 0x2000
	s_add_u32 s88, s56, 0x40000
	v_lshl_add_u64 v[222:223], s[56:57], 0, v[152:153]
	s_addc_u32 s89, s57, 0
	s_add_i32 s87, s80, s66
	global_load_lds_dwordx4 v[222:223], off
	v_lshl_add_u64 v[140:141], s[88:89], 0, v[148:149]
	s_mov_b32 m0, s87
	v_lshl_add_u64 v[224:225], s[58:59], 0, v[146:147]
	global_load_lds_dwordx4 v[140:141], off
	v_lshl_add_u64 v[140:141], s[88:89], 0, v[152:153]
	s_add_i32 m0, s87, 0x2000
	v_lshl_add_u64 v[226:227], s[58:59], 0, v[150:151]
	global_load_lds_dwordx4 v[140:141], off
	s_mov_b32 m0, s51
	s_nop 0
	global_load_lds_dwordx4 v[224:225], off
	s_mov_b32 m0, s67
	s_nop 0
	global_load_lds_dwordx4 v[226:227], off
	s_waitcnt vmcnt(8)
	s_waitcnt lgkmcnt(0)
	s_barrier
; #define PG8_STAGE(bufoff, gbase, voff) do { _Pragma("unroll") for (int _i = 0; _i < 2; ++_i) \
;         __builtin_amdgcn_global_load_lds((const unsigned*)((const char*)(gbase) + (voff)[_i]), (PG8_LAS unsigned*)(lds + (bufoff) + ldsw + _i * 8192), 16, 0, 0); } while (0)
; #define PG8_STAGE_A(bufoff, kbase, h, gv) do { if constexpr (GATHER) { PG8_STAGE(bufoff, kbase, (gv)[h]); } else { PG8_STAGE(bufoff, (kbase) + (h) * hstep, voffA); } } while (0)
; #define PG8_WAIT_V(n) asm volatile("s_waitcnt vmcnt(" #n ")" ::: "memory")
; #define PG8_WAIT_L(n) asm volatile("s_waitcnt lgkmcnt(" #n ")" ::: "memory")
; #define PG8_BAR __builtin_amdgcn_s_barrier()
; #define PG8_SCHED __builtin_amdgcn_sched_barrier(0)
; template <class Epi, class Sched, bool ALIGN_EPI = false, bool SP2 = false, bool FP8 = false, bool GATHER = false>
; __device__ __forceinline__ void gemm_phase(PG8_LAS unsigned char* lds, const Gemm g, const Sched& S, const Epi& E) {
;     ...
;             PG8_WAIT_V(8); PG8_WAIT_L(0); PG8_BAR; PG8_MMA(1, 0, At, B0); PG8_MMA(1, 1, At, B1); PG8_BAR; PG8_SCHED;
;             PG8_LDB(B0, 1, 0); PG8_LDB(B1, 1, 1); PG8_SCHED; PG8_LDA(At, 1, 0); PG8_STAGE_A(PG8_SA(0, 1), a2, 1, gsel);
;             PG8_WAIT_V(8); PG8_WAIT_L(0); PG8_BAR; PG8_MMA(0, 0, At, B0); PG8_MMA(0, 1, At, B1); PG8_BAR; PG8_SCHED;
;             PG8_LDA(At, 1, 1); PG8_STAGE(PG8_SB(1, 0), b3, voffB); PG8_STAGE(PG8_SB(1, 1), b3 + hstep, voffB); PG8_STAGE_A(PG8_SA(1, 0), a3, 0, gsel);
	s_setprio 1
	s_waitcnt lgkmcnt(0)
	v_mfma_f32_16x16x32_bf16 v[62:65], v[124:127], v[188:191], 0
	v_mfma_f32_16x16x32_bf16 v[58:61], v[132:135], v[188:191], 0
	v_mfma_f32_16x16x32_bf16 v[54:57], v[124:127], v[196:199], 0
	v_mfma_f32_16x16x32_bf16 v[42:45], v[132:135], v[196:199], 0
	v_mfma_f32_16x16x32_bf16 v[38:41], v[124:127], v[204:207], 0
	v_mfma_f32_16x16x32_bf16 v[26:29], v[132:135], v[204:207], 0
	v_mfma_f32_16x16x32_bf16 v[22:25], v[124:127], v[212:215], 0
	v_mfma_f32_16x16x32_bf16 v[10:13], v[132:135], v[212:215], 0
	v_mfma_f32_16x16x32_bf16 v[62:65], v[128:131], v[192:195], v[62:65]
	v_mfma_f32_16x16x32_bf16 v[58:61], v[164:167], v[192:195], v[58:61]
	v_mfma_f32_16x16x32_bf16 v[54:57], v[128:131], v[200:203], v[54:57]
	v_mfma_f32_16x16x32_bf16 v[42:45], v[164:167], v[200:203], v[42:45]
	v_mfma_f32_16x16x32_bf16 v[38:41], v[128:131], v[208:211], v[38:41]
	v_mfma_f32_16x16x32_bf16 v[26:29], v[164:167], v[208:211], v[26:29]
	v_mfma_f32_16x16x32_bf16 v[22:25], v[128:131], v[216:219], v[22:25]
	v_mfma_f32_16x16x32_bf16 v[10:13], v[164:167], v[216:219], v[10:13]
	s_setprio 0
	s_setprio 1
	v_mfma_f32_16x16x32_bf16 v[50:53], v[172:175], v[188:191], 0
	v_mfma_f32_16x16x32_bf16 v[46:49], v[180:183], v[188:191], 0
	v_mfma_f32_16x16x32_bf16 v[34:37], v[172:175], v[196:199], 0
	v_mfma_f32_16x16x32_bf16 v[30:33], v[180:183], v[196:199], 0
	v_mfma_f32_16x16x32_bf16 v[18:21], v[172:175], v[204:207], 0
	v_mfma_f32_16x16x32_bf16 v[14:17], v[180:183], v[204:207], 0
	v_mfma_f32_16x16x32_bf16 v[6:9], v[172:175], v[212:215], 0
	v_mfma_f32_16x16x32_bf16 v[2:5], v[180:183], v[212:215], 0
	v_mfma_f32_16x16x32_bf16 v[50:53], v[176:179], v[192:195], v[50:53]
	v_mfma_f32_16x16x32_bf16 v[46:49], v[184:187], v[192:195], v[46:49]
	v_mfma_f32_16x16x32_bf16 v[34:37], v[176:179], v[200:203], v[34:37]
	v_mfma_f32_16x16x32_bf16 v[30:33], v[184:187], v[200:203], v[30:33]
	v_mfma_f32_16x16x32_bf16 v[18:21], v[176:179], v[208:211], v[18:21]
	v_mfma_f32_16x16x32_bf16 v[14:17], v[184:187], v[208:211], v[14:17]
	v_mfma_f32_16x16x32_bf16 v[6:9], v[176:179], v[216:219], v[6:9]
	v_mfma_f32_16x16x32_bf16 v[2:5], v[184:187], v[216:219], v[2:5]
	s_setprio 0
	s_barrier
	s_add_i32 s87, 0, 0x18000
	v_add_u32_e32 v140, s87, v169
	s_add_i32 s88, 0, 0x1c000
	ds_read_b128 v[124:127], v140
	ds_read_b128 v[128:131], v140 offset:1024
	ds_read_b128 v[132:135], v140 offset:2048
	ds_read_b128 v[164:167], v140 offset:3072
	v_add_u32_e32 v140, s88, v169
	ds_read_b128 v[172:175], v140
	ds_read_b128 v[176:179], v140 offset:1024
	ds_read_b128 v[180:183], v140 offset:2048
	ds_read_b128 v[184:187], v140 offset:3072
	s_add_u32 s58, s58, 0x40000
	s_addc_u32 s59, s59, 0
	s_mov_b32 m0, s68
	v_lshl_add_u64 v[140:141], s[58:59], 0, v[146:147]
	ds_read_b128 v[188:191], v170 offset:32768
	ds_read_b128 v[192:195], v170 offset:33792
	ds_read_b128 v[196:199], v170 offset:34816
	ds_read_b128 v[200:203], v170 offset:35840
	ds_read_b128 v[204:207], v170 offset:36864
	ds_read_b128 v[208:211], v170 offset:37888
	ds_read_b128 v[212:215], v170 offset:38912
	ds_read_b128 v[216:219], v170 offset:39936
	global_load_lds_dwordx4 v[140:141], off
	v_lshl_add_u64 v[140:141], s[58:59], 0, v[150:151]
	s_mov_b32 m0, s69
	s_nop 0
	global_load_lds_dwordx4 v[140:141], off
	s_waitcnt vmcnt(8)
	s_waitcnt lgkmcnt(0)
	s_barrier
	s_setprio 1
	s_waitcnt lgkmcnt(0)
	v_mfma_f32_16x16x32_bf16 v[140:143], v[124:127], v[188:191], v[142:145]
	v_mfma_f32_16x16x32_bf16 v[136:139], v[132:135], v[188:191], v[136:139]
	v_mfma_f32_16x16x32_bf16 v[118:121], v[124:127], v[196:199], v[118:121]
	v_mfma_f32_16x16x32_bf16 v[106:109], v[132:135], v[196:199], v[106:109]
	v_mfma_f32_16x16x32_bf16 v[102:105], v[124:127], v[204:207], v[102:105]
	v_mfma_f32_16x16x32_bf16 v[90:93], v[132:135], v[204:207], v[90:93]
	v_mfma_f32_16x16x32_bf16 v[86:89], v[124:127], v[212:215], v[86:89]
	v_mfma_f32_16x16x32_bf16 v[74:77], v[132:135], v[212:215], v[74:77]
	v_mfma_f32_16x16x32_bf16 v[142:145], v[128:131], v[192:195], v[140:143]
	v_mfma_f32_16x16x32_bf16 v[138:141], v[164:167], v[192:195], v[136:139]
	v_mfma_f32_16x16x32_bf16 v[118:121], v[128:131], v[200:203], v[118:121]
	v_mfma_f32_16x16x32_bf16 v[106:109], v[164:167], v[200:203], v[106:109]
	v_mfma_f32_16x16x32_bf16 v[102:105], v[128:131], v[208:211], v[102:105]
	v_mfma_f32_16x16x32_bf16 v[90:93], v[164:167], v[208:211], v[90:93]
	v_mfma_f32_16x16x32_bf16 v[86:89], v[128:131], v[216:219], v[86:89]
	v_mfma_f32_16x16x32_bf16 v[74:77], v[164:167], v[216:219], v[74:77]
	s_setprio 0
	s_setprio 1
	v_mfma_f32_16x16x32_bf16 v[114:117], v[172:175], v[188:191], v[114:117]
	v_mfma_f32_16x16x32_bf16 v[110:113], v[180:183], v[188:191], v[110:113]
	v_mfma_f32_16x16x32_bf16 v[98:101], v[172:175], v[196:199], v[98:101]
	v_mfma_f32_16x16x32_bf16 v[94:97], v[180:183], v[196:199], v[94:97]
	v_mfma_f32_16x16x32_bf16 v[82:85], v[172:175], v[204:207], v[82:85]
	v_mfma_f32_16x16x32_bf16 v[78:81], v[180:183], v[204:207], v[78:81]
	v_mfma_f32_16x16x32_bf16 v[70:73], v[172:175], v[212:215], v[70:73]
	v_mfma_f32_16x16x32_bf16 v[66:69], v[180:183], v[212:215], v[66:69]
	v_mfma_f32_16x16x32_bf16 v[114:117], v[176:179], v[192:195], v[114:117]
	v_mfma_f32_16x16x32_bf16 v[110:113], v[184:187], v[192:195], v[110:113]
	v_mfma_f32_16x16x32_bf16 v[98:101], v[176:179], v[200:203], v[98:101]
	v_mfma_f32_16x16x32_bf16 v[94:97], v[184:187], v[200:203], v[94:97]
	v_mfma_f32_16x16x32_bf16 v[82:85], v[176:179], v[208:211], v[82:85]
	v_mfma_f32_16x16x32_bf16 v[78:81], v[184:187], v[208:211], v[78:81]
	v_mfma_f32_16x16x32_bf16 v[70:73], v[176:179], v[216:219], v[70:73]
	v_mfma_f32_16x16x32_bf16 v[66:69], v[184:187], v[216:219], v[66:69]
	s_setprio 0
	s_barrier
; #define PG8_STAGE(bufoff, gbase, voff) do { _Pragma("unroll") for (int _i = 0; _i < 2; ++_i) \
;         __builtin_amdgcn_global_load_lds((const unsigned*)((const char*)(gbase) + (voff)[_i]), (PG8_LAS unsigned*)(lds + (bufoff) + ldsw + _i * 8192), 16, 0, 0); } while (0)
; #define PG8_STAGE_A(bufoff, kbase, h, gv) do { if constexpr (GATHER) { PG8_STAGE(bufoff, kbase, (gv)[h]); } else { PG8_STAGE(bufoff, (kbase) + (h) * hstep, voffA); } } while (0)
; #define PG8_WAIT_V(n) asm volatile("s_waitcnt vmcnt(" #n ")" ::: "memory")
; #define PG8_WAIT_L(n) asm volatile("s_waitcnt lgkmcnt(" #n ")" ::: "memory")
; #define PG8_BAR __builtin_amdgcn_s_barrier()
; #define PG8_SCHED __builtin_amdgcn_sched_barrier(0)
; template <class Epi, class Sched, bool ALIGN_EPI = false, bool SP2 = false, bool FP8 = false, bool GATHER = false>
; __device__ __forceinline__ void gemm_phase(PG8_LAS unsigned char* lds, const Gemm g, const Sched& S, const Epi& E) {
;     ...
;         for (int t = 0; t < nt; t += 2) {
;             const bool last = (t == nt - 2);
;             const char* a1 = cA + (size_t)(t + 1) * kstep;
;             const char* a2 = last ? nA : cA + (size_t)(t + 2) * kstep; const char* b2 = last ? nB : cB + (size_t)(t + 2) * kstep;
;             const char* a3 = a2 + kstep; const char* b3 = b2 + kstep;
;             if (last && has_next) S.a_ready(nxt);
;             if (last) E.pre(cur, wid, lane);
;     ...
;             PG8_LDA(At, 1, 1); PG8_STAGE(PG8_SB(1, 0), b3, voffB); PG8_STAGE(PG8_SB(1, 1), b3 + hstep, voffB); PG8_STAGE_A(PG8_SA(1, 0), a3, 0, gsel);
;             PG8_WAIT_V(8); PG8_WAIT_L(0); PG8_BAR; PG8_MMA(1, 0, At, B0); PG8_MMA(1, 1, At, B1); PG8_BAR; PG8_SCHED;
	s_add_i32 s58, s87, s66
	v_lshl_add_u64 v[136:137], v[220:221], 0, s[16:17]
	s_mov_b32 m0, s58
	ds_read_b128 v[188:191], v170 offset:49152
	ds_read_b128 v[192:195], v170 offset:50176
	ds_read_b128 v[196:199], v170 offset:51200
	ds_read_b128 v[200:203], v170 offset:52224
	ds_read_b128 v[204:207], v170 offset:53248
	ds_read_b128 v[208:211], v170 offset:54272
	ds_read_b128 v[212:215], v170 offset:55296
	ds_read_b128 v[216:219], v170 offset:56320
	global_load_lds_dwordx4 v[136:137], off
	s_add_i32 m0, s58, 0x2000
	s_add_u32 s56, s56, 0x40080
	v_lshl_add_u64 v[136:137], v[222:223], 0, s[16:17]
	s_addc_u32 s57, s57, 0
	s_add_i32 s58, s88, s66
	global_load_lds_dwordx4 v[136:137], off
	v_lshl_add_u64 v[136:137], s[56:57], 0, v[148:149]
	s_mov_b32 m0, s58
	s_nop 0
	global_load_lds_dwordx4 v[136:137], off
	v_lshl_add_u64 v[136:137], s[56:57], 0, v[152:153]
	s_add_i32 m0, s58, 0x2000
	s_nop 0
	global_load_lds_dwordx4 v[136:137], off
	v_lshl_add_u64 v[136:137], v[224:225], 0, s[16:17]
	s_mov_b32 m0, s75
	s_nop 0
	global_load_lds_dwordx4 v[136:137], off
	v_lshl_add_u64 v[136:137], v[226:227], 0, s[16:17]
	s_mov_b32 m0, s76
	s_nop 0
	global_load_lds_dwordx4 v[136:137], off
	s_waitcnt vmcnt(8)
	s_waitcnt lgkmcnt(0)
	s_barrier
	s_setprio 1
	s_waitcnt lgkmcnt(0)
	v_mfma_f32_16x16x32_bf16 v[62:65], v[124:127], v[188:191], v[62:65]
	v_mfma_f32_16x16x32_bf16 v[58:61], v[132:135], v[188:191], v[58:61]
	v_mfma_f32_16x16x32_bf16 v[54:57], v[124:127], v[196:199], v[54:57]
	v_mfma_f32_16x16x32_bf16 v[42:45], v[132:135], v[196:199], v[42:45]
	v_mfma_f32_16x16x32_bf16 v[38:41], v[124:127], v[204:207], v[38:41]
	v_mfma_f32_16x16x32_bf16 v[26:29], v[132:135], v[204:207], v[26:29]
	v_mfma_f32_16x16x32_bf16 v[22:25], v[124:127], v[212:215], v[22:25]
	v_mfma_f32_16x16x32_bf16 v[10:13], v[132:135], v[212:215], v[10:13]
	v_mfma_f32_16x16x32_bf16 v[62:65], v[128:131], v[192:195], v[62:65]
	v_mfma_f32_16x16x32_bf16 v[58:61], v[164:167], v[192:195], v[58:61]
	v_mfma_f32_16x16x32_bf16 v[54:57], v[128:131], v[200:203], v[54:57]
	v_mfma_f32_16x16x32_bf16 v[42:45], v[164:167], v[200:203], v[42:45]
	v_mfma_f32_16x16x32_bf16 v[38:41], v[128:131], v[208:211], v[38:41]
	v_mfma_f32_16x16x32_bf16 v[26:29], v[164:167], v[208:211], v[26:29]
	v_mfma_f32_16x16x32_bf16 v[22:25], v[128:131], v[216:219], v[22:25]
	v_mfma_f32_16x16x32_bf16 v[10:13], v[164:167], v[216:219], v[10:13]
	s_setprio 0
	s_setprio 1
	v_mfma_f32_16x16x32_bf16 v[50:53], v[172:175], v[188:191], v[50:53]
	v_mfma_f32_16x16x32_bf16 v[46:49], v[180:183], v[188:191], v[46:49]
	v_mfma_f32_16x16x32_bf16 v[34:37], v[172:175], v[196:199], v[34:37]
	v_mfma_f32_16x16x32_bf16 v[30:33], v[180:183], v[196:199], v[30:33]
	v_mfma_f32_16x16x32_bf16 v[18:21], v[172:175], v[204:207], v[18:21]
	v_mfma_f32_16x16x32_bf16 v[14:17], v[180:183], v[204:207], v[14:17]
	v_mfma_f32_16x16x32_bf16 v[6:9], v[172:175], v[212:215], v[6:9]
	v_mfma_f32_16x16x32_bf16 v[2:5], v[180:183], v[212:215], v[2:5]
	v_mfma_f32_16x16x32_bf16 v[50:53], v[176:179], v[192:195], v[50:53]
	v_mfma_f32_16x16x32_bf16 v[46:49], v[184:187], v[192:195], v[46:49]
	v_mfma_f32_16x16x32_bf16 v[34:37], v[176:179], v[200:203], v[34:37]
	v_mfma_f32_16x16x32_bf16 v[30:33], v[184:187], v[200:203], v[30:33]
	v_mfma_f32_16x16x32_bf16 v[18:21], v[176:179], v[208:211], v[18:21]
	v_mfma_f32_16x16x32_bf16 v[14:17], v[184:187], v[208:211], v[14:17]
	v_mfma_f32_16x16x32_bf16 v[6:9], v[176:179], v[216:219], v[6:9]
	v_mfma_f32_16x16x32_bf16 v[2:5], v[184:187], v[216:219], v[2:5]
	s_setprio 0
	s_add_i32 s86, s86, 2
	s_add_u32 s54, s54, 0x100
	s_addc_u32 s55, s55, 0
	s_add_u32 s53, s53, 0x100
	s_addc_u32 s85, s85, 0
	s_cmp_gt_u32 s86, 13
	s_cbranch_scc1 .Lrot1497_exit
	s_cmp_lg_u32 s86, 12
	s_cselect_b64 s[56:57], -1, 0
	s_or_b64 s[58:59], s[56:57], s[18:19]
	s_and_b64 vcc, exec, s[58:59]
	s_cbranch_vccnz .Lrot1497_head
	s_barrier
	s_branch .LBB0_1498
